# late weight prep: PEER-fold key-tile loop issues both tiles' row loads together (second tile in fresh registers), counted waits adjusted
# speedup vs baseline: 1.0026x; 1.0013x over previous
; __device__ __forceinline__ unsigned f2bf(float f) { unsigned u = __builtin_bit_cast(unsigned, f); return (u + 0x7fffu + ((u >> 16) & 1u)) >> 16; }
; __device__ __forceinline__ unsigned pk2(float lo, float hi) { return f2bf(lo) | (f2bf(hi) << 16); }
; __device__ __forceinline__ void late_weight_prep(const Params& P, LAS unsigned char* lds, int lane, int wave, int gw, int NGW) {
;     ...
;         for (int it = gw; it < 16 * 64; it += NGW) {
;             const int hp = it >> 6, k0 = (it & 63) * 16;
;             bf16x8 bq[4];
; #pragma unroll
;             for (int s = 0; s < 4; ++s) { const f32x4* src = (const f32x4*)(P.peer_wq + (size_t)(k0 + col) * 2048 + hp * 128 + 32 * s + 8 * g);
;                 const f32x4 a = src[0], c = src[1]; v4u pk; pk.x = pk2(a.x, a.y); pk.y = pk2(a.z, a.w); pk.z = pk2(c.x, c.y); pk.w = pk2(c.z, c.w); bq[s] = __builtin_bit_cast(bf16x8, pk); }
;             const float nw = P.norm_ffn_w[k0 + col];
; #pragma unroll 2
;             for (int kt = 0; kt < 8; ++kt) {
;                 f32x4 acc = (f32x4){0.f, 0.f, 0.f, 0.f};
; #pragma unroll
;                 for (int s = 0; s < 4; ++s) { const f32x4* src = (const f32x4*)(P.peer_subkeys + (size_t)(hp * 128 + 16 * kt + col) * 128 + 32 * s + 8 * g);
;                     const f32x4 a = src[0], c = src[1]; v4u pk; pk.x = pk2(a.x, a.y); pk.y = pk2(a.z, a.w); pk.z = pk2(c.x, c.y); pk.w = pk2(c.z, c.w);
;                     acc = __builtin_amdgcn_mfma_f32_16x16x32_bf16(__builtin_bit_cast(bf16x8, pk), bq[s], acc, 0, 0, 0); }
; #pragma unroll
;                 for (int i = 0; i < 4; ++i) WF[(size_t)(hp * 128 + 16 * kt + 4 * g + i) * 1024 + k0 + col] = (bf16)f2bf(acc[i] * nw);
.LBB0_2011:
	v_add_u32_e32 v30, s0, v1
	v_add_u32_e32 v34, s0, v22
	v_ashrrev_i32_e32 v31, 31, v30
	v_ashrrev_i32_e32 v35, 31, v34
	v_add_u32_e32 v36, 1, v34
	v_add_u32_e32 v38, 2, v34
	v_add_u32_e32 v40, 3, v34
	v_add_u32_e32 v42, 16, v30
	v_add_u32_e32 v44, 16, v34
	v_add_u32_e32 v46, 17, v34
	v_add_u32_e32 v48, 18, v34
	v_add_u32_e32 v50, 19, v34
	v_lshlrev_b64 v[30:31], 9, v[30:31]
	v_lshlrev_b64 v[34:35], 11, v[34:35]
	v_ashrrev_i32_e32 v37, 31, v36
	v_ashrrev_i32_e32 v39, 31, v38
	v_ashrrev_i32_e32 v41, 31, v40
	v_ashrrev_i32_e32 v43, 31, v42
	v_ashrrev_i32_e32 v45, 31, v44
	v_ashrrev_i32_e32 v47, 31, v46
	v_ashrrev_i32_e32 v49, 31, v48
	v_ashrrev_i32_e32 v51, 31, v50
	v_lshl_add_u64 v[30:31], v[24:25], 0, v[30:31]
	v_lshl_add_u64 v[66:67], v[28:29], 0, v[34:35]
	v_lshlrev_b64 v[68:69], 11, v[36:37]
	v_lshlrev_b64 v[70:71], 11, v[38:39]
	v_lshlrev_b64 v[72:73], 11, v[40:41]
	v_lshlrev_b64 v[74:75], 9, v[42:43]
	v_lshlrev_b64 v[76:77], 11, v[44:45]
	v_lshlrev_b64 v[78:79], 11, v[46:47]
	v_lshlrev_b64 v[80:81], 11, v[48:49]
	v_lshlrev_b64 v[82:83], 11, v[50:51]
	global_load_dwordx4 v[34:37], v[30:31], off
	global_load_dwordx4 v[38:41], v[30:31], off offset:16
	global_load_dwordx4 v[42:45], v[30:31], off offset:128
	global_load_dwordx4 v[46:49], v[30:31], off offset:144
	global_load_dwordx4 v[50:53], v[30:31], off offset:256
	global_load_dwordx4 v[54:57], v[30:31], off offset:272
	global_load_dwordx4 v[58:61], v[30:31], off offset:384
	global_load_dwordx4 v[62:65], v[30:31], off offset:400
	v_lshl_add_u64 v[30:31], v[28:29], 0, v[68:69]
	v_lshl_add_u64 v[68:69], v[28:29], 0, v[70:71]
	v_lshl_add_u64 v[70:71], v[28:29], 0, v[72:73]
	v_lshl_add_u64 v[72:73], v[24:25], 0, v[74:75]
	v_lshl_add_u64 v[74:75], v[28:29], 0, v[76:77]
	v_lshl_add_u64 v[76:77], v[28:29], 0, v[78:79]
	v_lshl_add_u64 v[78:79], v[28:29], 0, v[80:81]
	v_lshl_add_u64 v[80:81], v[28:29], 0, v[82:83]
	global_load_dwordx4 v[148:151], v[72:73], off
	global_load_dwordx4 v[152:155], v[72:73], off offset:16
	global_load_dwordx4 v[156:159], v[72:73], off offset:128
	global_load_dwordx4 v[160:163], v[72:73], off offset:144
	global_load_dwordx4 v[164:167], v[72:73], off offset:256
	global_load_dwordx4 v[168:171], v[72:73], off offset:272
	global_load_dwordx4 v[172:175], v[72:73], off offset:384
	global_load_dwordx4 v[176:179], v[72:73], off offset:400
	s_add_i32 s0, s0, 32
	s_cmpk_lg_i32 s0, 0x80
	s_waitcnt vmcnt(15)
	v_bfe_u32 v33, v34, 16, 1
	v_bfe_u32 v82, v35, 16, 1
	v_bfe_u32 v83, v36, 16, 1
	v_bfe_u32 v84, v37, 16, 1
	s_waitcnt vmcnt(14)
	v_bfe_u32 v85, v38, 16, 1
	v_bfe_u32 v86, v39, 16, 1
	v_bfe_u32 v87, v40, 16, 1
	v_bfe_u32 v88, v41, 16, 1
	v_add3_u32 v33, v34, v33, s7
	v_add3_u32 v34, v35, v82, s7
	v_add3_u32 v35, v36, v83, s7
	v_add3_u32 v36, v37, v84, s7
	v_add3_u32 v37, v38, v85, s7
	v_add3_u32 v38, v39, v86, s7
	v_add3_u32 v39, v40, v87, s7
	v_add3_u32 v40, v41, v88, s7
	v_lshrrev_b32_e32 v33, 16, v33
	v_lshrrev_b32_e32 v35, 16, v35
	v_lshrrev_b32_e32 v37, 16, v37
	v_lshrrev_b32_e32 v39, 16, v39
	v_and_or_b32 v34, v34, s13, v33
	v_and_or_b32 v35, v36, s13, v35
	v_and_or_b32 v36, v38, s13, v37
	v_and_or_b32 v37, v40, s13, v39
	s_waitcnt vmcnt(13)
	v_bfe_u32 v89, v42, 16, 1
	v_bfe_u32 v90, v43, 16, 1
	v_bfe_u32 v91, v44, 16, 1
	v_bfe_u32 v92, v45, 16, 1
	s_waitcnt vmcnt(12)
	v_bfe_u32 v93, v46, 16, 1
	v_bfe_u32 v94, v47, 16, 1
	v_bfe_u32 v95, v48, 16, 1
	v_bfe_u32 v96, v49, 16, 1
	v_add3_u32 v41, v42, v89, s7
	v_add3_u32 v42, v43, v90, s7
	v_add3_u32 v43, v44, v91, s7
	v_add3_u32 v44, v45, v92, s7
	v_add3_u32 v45, v46, v93, s7
	v_add3_u32 v46, v47, v94, s7
	v_add3_u32 v47, v48, v95, s7
	v_add3_u32 v48, v49, v96, s7
	v_lshrrev_b32_e32 v41, 16, v41
	v_lshrrev_b32_e32 v43, 16, v43
	v_lshrrev_b32_e32 v45, 16, v45
	v_lshrrev_b32_e32 v47, 16, v47
	v_and_or_b32 v38, v42, s13, v41
	v_and_or_b32 v39, v44, s13, v43
	v_and_or_b32 v40, v46, s13, v45
	v_and_or_b32 v41, v48, s13, v47
	s_waitcnt vmcnt(11)
	v_bfe_u32 v97, v50, 16, 1
	v_bfe_u32 v98, v51, 16, 1
	v_bfe_u32 v99, v52, 16, 1
	v_bfe_u32 v100, v53, 16, 1
	s_waitcnt vmcnt(10)
	v_bfe_u32 v101, v54, 16, 1
	v_bfe_u32 v102, v55, 16, 1
	v_bfe_u32 v103, v56, 16, 1
	v_mfma_f32_16x16x32_bf16 v[34:37], v[34:37], v[2:5], 0
	v_bfe_u32 v104, v57, 16, 1
	v_add3_u32 v49, v50, v97, s7
	v_add3_u32 v50, v51, v98, s7
	v_add3_u32 v51, v52, v99, s7
	v_add3_u32 v52, v53, v100, s7
	v_add3_u32 v53, v54, v101, s7
	v_add3_u32 v54, v55, v102, s7
	v_add3_u32 v55, v56, v103, s7
	v_add3_u32 v56, v57, v104, s7
	v_lshrrev_b32_e32 v49, 16, v49
	v_lshrrev_b32_e32 v51, 16, v51
	v_lshrrev_b32_e32 v53, 16, v53
	v_lshrrev_b32_e32 v55, 16, v55
	v_and_or_b32 v42, v50, s13, v49
	v_and_or_b32 v43, v52, s13, v51
	v_and_or_b32 v44, v54, s13, v53
	v_and_or_b32 v45, v56, s13, v55
	s_waitcnt vmcnt(9)
	v_bfe_u32 v105, v58, 16, 1
	v_bfe_u32 v106, v59, 16, 1
	v_bfe_u32 v107, v60, 16, 1
	v_bfe_u32 v108, v61, 16, 1
	s_waitcnt vmcnt(8)
; __device__ __forceinline__ unsigned f2bf(float f) { unsigned u = __builtin_bit_cast(unsigned, f); return (u + 0x7fffu + ((u >> 16) & 1u)) >> 16; }
; __device__ __forceinline__ unsigned pk2(float lo, float hi) { return f2bf(lo) | (f2bf(hi) << 16); }
; __device__ __forceinline__ void late_weight_prep(const Params& P, LAS unsigned char* lds, int lane, int wave, int gw, int NGW) {
;     ...
;             for (int kt = 0; kt < 8; ++kt) {
;                 f32x4 acc = (f32x4){0.f, 0.f, 0.f, 0.f};
; #pragma unroll
;                 for (int s = 0; s < 4; ++s) { const f32x4* src = (const f32x4*)(P.peer_subkeys + (size_t)(hp * 128 + 16 * kt + col) * 128 + 32 * s + 8 * g);
;                     const f32x4 a = src[0], c = src[1]; v4u pk; pk.x = pk2(a.x, a.y); pk.y = pk2(a.z, a.w); pk.z = pk2(c.x, c.y); pk.w = pk2(c.z, c.w);
;                     acc = __builtin_amdgcn_mfma_f32_16x16x32_bf16(__builtin_bit_cast(bf16x8, pk), bq[s], acc, 0, 0, 0); }
; #pragma unroll
;                 for (int i = 0; i < 4; ++i) WF[(size_t)(hp * 128 + 16 * kt + 4 * g + i) * 1024 + k0 + col] = (bf16)f2bf(acc[i] * nw);
;             }
;         }
	v_bfe_u32 v109, v62, 16, 1
	v_bfe_u32 v110, v63, 16, 1
	v_bfe_u32 v111, v64, 16, 1
	v_mfma_f32_16x16x32_bf16 v[34:37], v[38:41], v[6:9], v[34:37]
	v_bfe_u32 v112, v65, 16, 1
	v_add3_u32 v57, v58, v105, s7
	v_add3_u32 v58, v59, v106, s7
	v_add3_u32 v59, v60, v107, s7
	v_add3_u32 v60, v61, v108, s7
	v_add3_u32 v61, v62, v109, s7
	v_add3_u32 v62, v63, v110, s7
	v_add3_u32 v63, v64, v111, s7
	v_add3_u32 v64, v65, v112, s7
	v_lshrrev_b32_e32 v57, 16, v57
	v_lshrrev_b32_e32 v59, 16, v59
	v_lshrrev_b32_e32 v61, 16, v61
	v_lshrrev_b32_e32 v63, 16, v63
	v_and_or_b32 v38, v58, s13, v57
	v_and_or_b32 v39, v60, s13, v59
	v_and_or_b32 v40, v62, s13, v61
	v_and_or_b32 v41, v64, s13, v63
	v_mfma_f32_16x16x32_bf16 v[34:37], v[42:45], v[10:13], v[34:37]
	s_nop 0
	v_mfma_f32_16x16x32_bf16 v[34:37], v[38:41], v[14:17], v[34:37]
	s_nop 7
	v_mul_f32_e32 v33, v32, v34
	v_mul_f32_e32 v34, v32, v35
	v_mul_f32_e32 v35, v32, v36
	v_mul_f32_e32 v36, v32, v37
	v_bfe_u32 v37, v33, 16, 1
	v_bfe_u32 v38, v34, 16, 1
	v_bfe_u32 v39, v35, 16, 1
	v_bfe_u32 v40, v36, 16, 1
	v_add3_u32 v33, v33, v37, s7
	v_add3_u32 v34, v34, v38, s7
	v_add3_u32 v35, v35, v39, s7
	v_add3_u32 v36, v36, v40, s7
	global_store_short_d16_hi v[66:67], v33, off
	global_store_short_d16_hi v[30:31], v34, off
	global_store_short_d16_hi v[68:69], v35, off
	global_store_short_d16_hi v[70:71], v36, off
	s_nop 0
	s_waitcnt vmcnt(11)
	v_bfe_u32 v30, v148, 16, 1
	v_bfe_u32 v31, v149, 16, 1
	v_bfe_u32 v33, v150, 16, 1
	v_bfe_u32 v66, v151, 16, 1
	s_waitcnt vmcnt(10)
	v_bfe_u32 v67, v152, 16, 1
	v_bfe_u32 v69, v154, 16, 1
	v_bfe_u32 v68, v153, 16, 1
	v_bfe_u32 v70, v155, 16, 1
	s_waitcnt vmcnt(9)
	v_bfe_u32 v71, v156, 16, 1
	v_bfe_u32 v82, v159, 16, 1
	s_waitcnt vmcnt(8)
	v_bfe_u32 v85, v162, 16, 1
	s_waitcnt vmcnt(7)
	v_bfe_u32 v88, v165, 16, 1
	s_waitcnt vmcnt(6)
	v_bfe_u32 v91, v168, 16, 1
	v_bfe_u32 v94, v171, 16, 1
	s_waitcnt vmcnt(5)
	v_bfe_u32 v97, v174, 16, 1
	s_waitcnt vmcnt(4)
	v_bfe_u32 v100, v177, 16, 1
	v_add3_u32 v30, v148, v30, s7
	v_add3_u32 v31, v149, v31, s7
	v_add3_u32 v33, v150, v33, s7
	v_add3_u32 v35, v151, v66, s7
	v_add3_u32 v34, v152, v67, s7
	v_add3_u32 v37, v154, v69, s7
	v_add3_u32 v36, v153, v68, s7
	v_add3_u32 v38, v155, v70, s7
	v_add3_u32 v39, v156, v71, s7
	v_add3_u32 v42, v159, v82, s7
	v_add3_u32 v45, v162, v85, s7
	v_add3_u32 v48, v165, v88, s7
	v_add3_u32 v51, v168, v91, s7
	v_add3_u32 v54, v171, v94, s7
	v_add3_u32 v57, v174, v97, s7
	v_add3_u32 v60, v177, v100, s7
	v_lshrrev_b32_e32 v30, 16, v30
	v_lshrrev_b32_e32 v33, 16, v33
	v_lshrrev_b32_e32 v63, 16, v34
	v_lshrrev_b32_e32 v37, 16, v37
	v_and_or_b32 v34, v31, s13, v30
	v_and_or_b32 v35, v35, s13, v33
	v_and_or_b32 v36, v36, s13, v63
	v_and_or_b32 v37, v38, s13, v37
	v_bfe_u32 v72, v157, 16, 1
	v_bfe_u32 v73, v158, 16, 1
	v_bfe_u32 v83, v160, 16, 1
	v_bfe_u32 v84, v161, 16, 1
	v_bfe_u32 v86, v163, 16, 1
	v_add3_u32 v40, v157, v72, s7
	v_add3_u32 v41, v158, v73, s7
	v_add3_u32 v43, v160, v83, s7
	v_add3_u32 v44, v161, v84, s7
	v_add3_u32 v46, v163, v86, s7
	v_lshrrev_b32_e32 v39, 16, v39
	v_lshrrev_b32_e32 v41, 16, v41
	v_lshrrev_b32_e32 v43, 16, v43
	v_lshrrev_b32_e32 v45, 16, v45
	v_and_or_b32 v38, v40, s13, v39
	v_and_or_b32 v39, v42, s13, v41
	v_and_or_b32 v40, v44, s13, v43
	v_and_or_b32 v41, v46, s13, v45
	v_bfe_u32 v87, v164, 16, 1
	v_bfe_u32 v89, v166, 16, 1
	v_bfe_u32 v90, v167, 16, 1
	v_bfe_u32 v93, v170, 16, 1
	v_mfma_f32_16x16x32_bf16 v[34:37], v[34:37], v[2:5], 0
	v_bfe_u32 v92, v169, 16, 1
	v_add3_u32 v47, v164, v87, s7
	v_add3_u32 v49, v166, v89, s7
	v_add3_u32 v50, v167, v90, s7
	v_add3_u32 v53, v170, v93, s7
	v_add3_u32 v52, v169, v92, s7
	v_lshrrev_b32_e32 v47, 16, v47
	v_lshrrev_b32_e32 v49, 16, v49
	v_lshrrev_b32_e32 v51, 16, v51
	v_lshrrev_b32_e32 v53, 16, v53
	v_and_or_b32 v42, v48, s13, v47
	v_and_or_b32 v43, v50, s13, v49
	v_and_or_b32 v44, v52, s13, v51
	v_and_or_b32 v45, v54, s13, v53
	v_bfe_u32 v95, v172, 16, 1
	v_bfe_u32 v96, v173, 16, 1
	v_bfe_u32 v98, v175, 16, 1
	v_bfe_u32 v99, v176, 16, 1
	v_bfe_u32 v101, v178, 16, 1
	v_mfma_f32_16x16x32_bf16 v[34:37], v[38:41], v[6:9], v[34:37]
	v_bfe_u32 v102, v179, 16, 1
	v_add3_u32 v55, v172, v95, s7
	v_add3_u32 v56, v173, v96, s7
	v_add3_u32 v58, v175, v98, s7
	v_add3_u32 v59, v176, v99, s7
	v_add3_u32 v61, v178, v101, s7
	v_add3_u32 v62, v179, v102, s7
	v_lshrrev_b32_e32 v55, 16, v55
	v_lshrrev_b32_e32 v57, 16, v57
	v_lshrrev_b32_e32 v59, 16, v59
	v_lshrrev_b32_e32 v61, 16, v61
	v_and_or_b32 v38, v56, s13, v55
	v_and_or_b32 v39, v58, s13, v57
	v_and_or_b32 v40, v60, s13, v59
	v_and_or_b32 v41, v62, s13, v61
	v_mfma_f32_16x16x32_bf16 v[34:37], v[42:45], v[10:13], v[34:37]
	s_nop 0
	v_mfma_f32_16x16x32_bf16 v[34:37], v[38:41], v[14:17], v[34:37]
	s_nop 7
	v_mul_f32_e32 v30, v32, v34
	v_mul_f32_e32 v31, v32, v35
	v_mul_f32_e32 v33, v32, v36
	v_mul_f32_e32 v34, v32, v37
	v_bfe_u32 v35, v30, 16, 1
	v_bfe_u32 v36, v31, 16, 1
	v_bfe_u32 v37, v33, 16, 1
	v_bfe_u32 v38, v34, 16, 1
	v_add3_u32 v30, v30, v35, s7
	v_add3_u32 v31, v31, v36, s7
	v_add3_u32 v33, v33, v37, s7
	v_add3_u32 v34, v34, v38, s7
	global_store_short_d16_hi v[74:75], v30, off
	global_store_short_d16_hi v[76:77], v31, off
	global_store_short_d16_hi v[78:79], v33, off
	global_store_short_d16_hi v[80:81], v34, off
	s_cbranch_scc1 .LBB0_2011
	s_add_i32 s19, s19, s18
	s_add_i32 s3, s3, s6
	s_cmpk_lt_i32 s19, 0x400
	s_cbranch_scc1 .LBB0_2010
